# mix1: 256 (was 384) expert-weight conversion tiles on the attention workgroups - one each
# baseline (speedup 1.0000x reference)
; #define PR_BEGIN(id) do { if (PROBE_SP == (id)) c.prt = __builtin_amdgcn_s_memrealtime(); } while (0)
; #define PR_END(id) do { if (PROBE_SP == (id)) c.pracc += __builtin_amdgcn_s_memrealtime() - c.prt; } while (0)
; __device__ __forceinline__ void ph_mix1(Ctx& c, int layer, int bid, int G, unsigned char* lds, const volatile unsigned* rolew) {
;     ...
;     if (c.tid == 0) { __builtin_amdgcn_fence(__ATOMIC_RELEASE, "agent"); asm volatile("s_waitcnt vmcnt(0)" ::: "memory"); (void)__hip_atomic_fetch_add(l1done, 1u, __ATOMIC_RELAXED, __HIP_MEMORY_SCOPE_AGENT); }
;     for (int t = idx; t < 576 + (CVT_MOE_TILES - CVT_H); t += nlight) {
;         asm volatile("" : "+v"(c.tid)); asm volatile("" : "+s"(c.p));
;         if (t < 576) { PR_BEGIN(134); attn_tile<-1>(c, layer, t + 512, lds); PR_END(134); }
;         else { PR_BEGIN(131); cvt_moe(c, layer, CVT_H + t - 576); PR_END(131); }
.LBB0_384:
	s_or_b64 exec, exec, s[6:7]
	s_cmpk_gt_i32 s63, 0x73f
	s_cbranch_scc1 .LBB0_432
	s_ashr_i32 s55, s54, 31
	s_lshl_b32 s6, s54, 2
	s_lshl_b64 s[42:43], s[54:55], 26
	v_writelane_b32 v251, s6, 14
	s_lshl_b32 s6, s54, 6
	s_mov_b32 s15, s63
	v_writelane_b32 v251, s6, 15
	s_branch .LBB0_388

; #define PR_BEGIN(id) do { if (PROBE_SP == (id)) c.prt = __builtin_amdgcn_s_memrealtime(); } while (0)
; #define PR_END(id) do { if (PROBE_SP == (id)) c.pracc += __builtin_amdgcn_s_memrealtime() - c.prt; } while (0)
;     template <class T> __device__ __forceinline__ T* w(size_t off) const { return (T*)(p->ws + off); }
; __device__ __forceinline__ void cvt_moe(const Ctx& c, int layer, int tile) {
;     ...
;     for (int h = 0; h < 2; ++h) {
;         gfp sp[8]; gbp dp[8];
;         if (tile < 1024) {
; #pragma unroll
;             for (int i = 0; i < 8; ++i) {
;                 const int it = tile * 4096 + (h * 8 + i) * 256 + c.tid;
;                 const int ch = it & 127, ek = it >> 7;
;                 const int blk = ch >> 3, w = (ch & 7) * 8;
;                 sp[i] = (w < 32 ? pg : pu) + ((size_t)layer * NEXP * D + ek) * DE + blk * 32 + (w & 31);
;                 dp[i] = (gbp)c.w<bf16>(WS_BGU) + (size_t)ek * 1024 + ch * 8;
;             }
; __device__ __forceinline__ void ph_mix1(Ctx& c, int layer, int bid, int G, unsigned char* lds, const volatile unsigned* rolew) {
;     ...
;     for (int t = idx; t < 576 + (CVT_MOE_TILES - CVT_H); t += nlight) {
;         asm volatile("" : "+v"(c.tid)); asm volatile("" : "+s"(c.p));
;         if (t < 576) { PR_BEGIN(134); attn_tile<-1>(c, layer, t + 512, lds); PR_END(134); }
;         else { PR_BEGIN(131); cvt_moe(c, layer, CVT_H + t - 576); PR_END(131); }
.LBB0_387:
	s_add_i32 s15, s15, s71
	s_cmpk_gt_i32 s15, 0x73f
	s_cbranch_scc1 .LBB0_432
.LBB0_388:
	s_mov_b64 s[6:7], -1
	s_cmpk_gt_i32 s15, 0x23f
	v_lshlrev_b32_e32 v38, 4, v147
	s_cbranch_scc0 .LBB0_395
	s_load_dwordx4 s[16:19], s[0:1], 0x108
	s_load_dwordx2 s[44:45], s[0:1], 0x118
	v_and_b32_e32 v2, 4, v147
	v_cmp_eq_u32_e32 vcc, 0, v2
	s_add_i32 s6, s15, 0xfffffec0
	s_cmpk_gt_u32 s6, 0x3ff
	s_waitcnt lgkmcnt(0)
	s_cselect_b64 s[28:29], -1, 0
	v_mov_b32_e32 v4, s19
	v_mov_b32_e32 v5, s17
	v_cndmask_b32_e32 v5, v4, v5, vcc
	v_mov_b32_e32 v2, s18
	v_mov_b32_e32 v4, s16
	v_cndmask_b32_e32 v4, v2, v4, vcc
	v_lshl_add_u64 v[4:5], v[4:5], 0, s[42:43]
	v_and_b32_e32 v2, 0x780, v38
	s_lshl_b32 s6, s6, 12
	v_lshl_add_u64 v[4:5], v[4:5], 0, v[2:3]
	v_lshlrev_b32_e32 v2, 5, v147
	s_add_i32 s7, s6, 0xffc00000
	v_and_b32_e32 v6, 0x7f, v147
	v_and_b32_e32 v2, 0x60, v2
	s_add_u32 s44, s44, s42
	v_lshl_add_u64 v[4:5], v[4:5], 0, v[2:3]
	v_lshlrev_b32_e32 v2, 3, v6
	s_addc_u32 s45, s45, s43
	v_add_u32_e32 v39, s7, v147
	s_mov_b32 s7, 0
	s_mov_b64 s[46:47], -1
	v_lshlrev_b32_e32 v2, 1, v2
	s_branch .LBB0_391

; #define PR_BEGIN(id) do { if (PROBE_SP == (id)) c.prt = __builtin_amdgcn_s_memrealtime(); } while (0)
; #define PR_END(id) do { if (PROBE_SP == (id)) c.pracc += __builtin_amdgcn_s_memrealtime() - c.prt; } while (0)
; __device__ __forceinline__ void ph_mix1(Ctx& c, int layer, int bid, int G, unsigned char* lds, const volatile unsigned* rolew) {
;     ...
;         for (int t = idx; t < 512; t += nheavy) { asm volatile("" : "+v"(c.tid)); asm volatile("" : "+s"(c.p)); PR_BEGIN(130); attn_tile<0>(c, layer, t, lds); PR_END(130); }
;         for (int t = idx; t < CVT_H; t += nheavy) { asm volatile("" : "+v"(c.tid)); asm volatile("" : "+s"(c.p)); PR_BEGIN(131); cvt_moe(c, layer, t); PR_END(131); }
.LBB0_455:
	s_cmpk_gt_i32 s63, 0xff
	s_cbranch_scc1 .LBB0_460
	s_ashr_i32 s55, s54, 31
	s_lshl_b64 s[28:29], s[54:55], 26
	s_mov_b32 s6, s63

; __device__ __forceinline__ unsigned pk2bf(float lo, float hi) { const f32x2 v = {lo, hi}; return __builtin_bit_cast(unsigned, __builtin_convertvector(v, bf16x2_t)); }
;     template <class T> __device__ __forceinline__ T* w(size_t off) const { return (T*)(p->ws + off); }
; __device__ __forceinline__ void cvt_moe(const Ctx& c, int layer, int tile) {
;     ...
;     for (int h = 0; h < 2; ++h) {
;         gfp sp[8]; gbp dp[8];
;         if (tile < 1024) {
; #pragma unroll
;             for (int i = 0; i < 8; ++i) {
;                 const int it = tile * 4096 + (h * 8 + i) * 256 + c.tid;
;                 const int ch = it & 127, ek = it >> 7;
;                 const int blk = ch >> 3, w = (ch & 7) * 8;
;                 sp[i] = (w < 32 ? pg : pu) + ((size_t)layer * NEXP * D + ek) * DE + blk * 32 + (w & 31);
;                 dp[i] = (gbp)c.w<bf16>(WS_BGU) + (size_t)ek * 1024 + ch * 8;
;             }
;         } else {
; #pragma unroll
;             for (int i = 0; i < 8; ++i) {
;                 const int j = tile * 4096 + (h * 8 + i) * 256 + c.tid - 32 * 1024 * 128;
;                 sp[i] = pd + (size_t)layer * NEXP * DE * D + (size_t)j * 8; dp[i] = (gbp)c.w<bf16>(WS_BDN) + (size_t)j * 8;
;             }
;         }
;         f32x4 va[8], vb[8];
; #pragma unroll
;         for (int i = 0; i < 8; ++i) { va[i] = *(const __attribute__((address_space(1))) f32x4*)sp[i]; vb[i] = *(const __attribute__((address_space(1))) f32x4*)(sp[i] + 4); }
; #pragma unroll
;         for (int i = 0; i < 8; ++i) { u32x4 o; o[0] = pk2bf(va[i][0], va[i][1]); o[1] = pk2bf(va[i][2], va[i][3]); o[2] = pk2bf(vb[i][0], vb[i][1]); o[3] = pk2bf(vb[i][2], vb[i][3]); *(__attribute__((address_space(1))) u32x4*)dp[i] = o; }
;     }
.LBB0_458:
	v_add_u32_e32 v2, s7, v8
	v_ashrrev_i32_e32 v10, 7, v2
	v_add_u32_e32 v9, 0x100, v2
	v_add_u32_e32 v13, 0x200, v2
	v_add_u32_e32 v15, 0x300, v2
	v_add_u32_e32 v17, 0x400, v2
	v_add_u32_e32 v19, 0x500, v2
	v_add_u32_e32 v21, 0x600, v2
	v_add_u32_e32 v2, 0x700, v2
	v_ashrrev_i32_e32 v11, 31, v10
	v_ashrrev_i32_e32 v12, 7, v9
	v_ashrrev_i32_e32 v14, 7, v13
	v_ashrrev_i32_e32 v16, 7, v15
	v_ashrrev_i32_e32 v18, 7, v17
	v_ashrrev_i32_e32 v20, 7, v19
	v_ashrrev_i32_e32 v22, 7, v21
	v_ashrrev_i32_e32 v24, 7, v2
	v_lshlrev_b64 v[74:75], 11, v[10:11]
	v_ashrrev_i32_e32 v13, 31, v12
	v_ashrrev_i32_e32 v15, 31, v14
	v_ashrrev_i32_e32 v17, 31, v16
	v_ashrrev_i32_e32 v19, 31, v18
	v_ashrrev_i32_e32 v21, 31, v20
	v_ashrrev_i32_e32 v23, 31, v22
	v_ashrrev_i32_e32 v25, 31, v24
	v_lshl_add_u64 v[26:27], v[4:5], 0, v[74:75]
	v_lshlrev_b64 v[76:77], 11, v[12:13]
	v_lshlrev_b64 v[78:79], 11, v[14:15]
	v_lshlrev_b64 v[80:81], 11, v[16:17]
	v_lshlrev_b64 v[82:83], 11, v[18:19]
	v_lshlrev_b64 v[84:85], 11, v[20:21]
	v_lshlrev_b64 v[86:87], 11, v[22:23]
	v_lshlrev_b64 v[88:89], 11, v[24:25]
	v_lshl_add_u64 v[22:23], v[4:5], 0, v[76:77]
	v_lshl_add_u64 v[30:31], v[4:5], 0, v[78:79]
	v_lshl_add_u64 v[38:39], v[4:5], 0, v[80:81]
	global_load_dwordx4 v[10:13], v[26:27], off offset:16
	global_load_dwordx4 v[14:17], v[26:27], off
	v_lshl_add_u64 v[46:47], v[4:5], 0, v[82:83]
	v_lshl_add_u64 v[54:55], v[4:5], 0, v[84:85]
	v_lshl_add_u64 v[62:63], v[4:5], 0, v[86:87]
	v_lshl_add_u64 v[70:71], v[4:5], 0, v[88:89]
	global_load_dwordx4 v[18:21], v[22:23], off
	s_nop 0
	global_load_dwordx4 v[22:25], v[22:23], off offset:16
	s_nop 0
	global_load_dwordx4 v[26:29], v[30:31], off
	s_nop 0
	global_load_dwordx4 v[30:33], v[30:31], off offset:16
	s_nop 0
	global_load_dwordx4 v[34:37], v[38:39], off
	s_nop 0
	global_load_dwordx4 v[38:41], v[38:39], off offset:16
	s_nop 0
	global_load_dwordx4 v[42:45], v[46:47], off
	s_nop 0
	global_load_dwordx4 v[46:49], v[46:47], off offset:16
	s_nop 0
	global_load_dwordx4 v[50:53], v[54:55], off
	s_nop 0
	global_load_dwordx4 v[54:57], v[54:55], off offset:16
	s_nop 0
	global_load_dwordx4 v[58:61], v[62:63], off
	s_nop 0
	global_load_dwordx4 v[62:65], v[62:63], off offset:16
	s_nop 0
	global_load_dwordx4 v[66:69], v[70:71], off
	s_nop 0
	global_load_dwordx4 v[70:73], v[70:71], off offset:16
	s_movk_i32 s7, 0x800
	s_and_b64 vcc, exec, s[42:43]
	s_mov_b64 s[42:43], 0
	v_lshl_add_u64 v[74:75], v[6:7], 0, v[74:75]
	v_lshl_add_u64 v[76:77], v[6:7], 0, v[76:77]
	v_lshl_add_u64 v[78:79], v[6:7], 0, v[78:79]
	v_lshl_add_u64 v[80:81], v[6:7], 0, v[80:81]
	v_lshl_add_u64 v[82:83], v[6:7], 0, v[82:83]
	v_lshl_add_u64 v[84:85], v[6:7], 0, v[84:85]
	v_lshl_add_u64 v[86:87], v[6:7], 0, v[86:87]
	v_lshl_add_u64 v[88:89], v[6:7], 0, v[88:89]
	s_waitcnt vmcnt(14)
	v_cvt_pk_bf16_f32 v14, v14, v15
	v_cvt_pk_bf16_f32 v15, v16, v17
	v_cvt_pk_bf16_f32 v16, v10, v11
	v_cvt_pk_bf16_f32 v17, v12, v13
	s_waitcnt vmcnt(13)
	v_cvt_pk_bf16_f32 v10, v18, v19
	v_cvt_pk_bf16_f32 v11, v20, v21
	s_waitcnt vmcnt(12)
	v_cvt_pk_bf16_f32 v12, v22, v23
	v_cvt_pk_bf16_f32 v13, v24, v25
	global_store_dwordx4 v[74:75], v[14:17], off
	s_waitcnt vmcnt(10)
	v_cvt_pk_bf16_f32 v18, v34, v35
	v_cvt_pk_bf16_f32 v19, v36, v37
	v_cvt_pk_bf16_f32 v14, v26, v27
	v_cvt_pk_bf16_f32 v15, v28, v29
	v_cvt_pk_bf16_f32 v16, v30, v31
	v_cvt_pk_bf16_f32 v17, v32, v33
	s_waitcnt vmcnt(9)
	v_cvt_pk_bf16_f32 v20, v38, v39
	v_cvt_pk_bf16_f32 v21, v40, v41
	s_waitcnt vmcnt(8)
	v_cvt_pk_bf16_f32 v22, v42, v43
	v_cvt_pk_bf16_f32 v23, v44, v45
	s_waitcnt vmcnt(7)
	v_cvt_pk_bf16_f32 v24, v46, v47
	v_cvt_pk_bf16_f32 v25, v48, v49
	s_waitcnt vmcnt(6)
	v_cvt_pk_bf16_f32 v26, v50, v51
	v_cvt_pk_bf16_f32 v27, v52, v53
	s_waitcnt vmcnt(5)
	v_cvt_pk_bf16_f32 v28, v54, v55
	v_cvt_pk_bf16_f32 v29, v56, v57
	s_waitcnt vmcnt(4)
	v_cvt_pk_bf16_f32 v30, v58, v59
	v_cvt_pk_bf16_f32 v31, v60, v61
	s_waitcnt vmcnt(3)
	v_cvt_pk_bf16_f32 v32, v62, v63
	v_cvt_pk_bf16_f32 v33, v64, v65
	s_waitcnt vmcnt(2)
	v_cvt_pk_bf16_f32 v34, v66, v67
	v_cvt_pk_bf16_f32 v35, v68, v69
	s_waitcnt vmcnt(1)
	v_cvt_pk_bf16_f32 v36, v70, v71
	v_cvt_pk_bf16_f32 v37, v72, v73
	global_store_dwordx4 v[76:77], v[10:13], off
	global_store_dwordx4 v[78:79], v[14:17], off
	global_store_dwordx4 v[80:81], v[18:21], off
	global_store_dwordx4 v[82:83], v[22:25], off
	global_store_dwordx4 v[84:85], v[26:29], off
	global_store_dwordx4 v[86:87], v[30:33], off
	global_store_dwordx4 v[88:89], v[34:37], off
	s_cbranch_vccnz .LBB0_458
	s_add_i32 s6, s6, s70
	s_cmpk_gt_i32 s6, 0xff
	s_cbranch_scc0 .LBB0_457
